# speedup vs baseline: 1.0286x; 1.0286x over previous
.LBB0_118:
	s_or_b64 exec, exec, s[60:61]
	v_readfirstlane_b32 s74, v0
	v_mov_b32_e32 v42, 0
	v_mov_b32_e32 v50, 0
	v_bfe_u32 v36, v0, 6, 2
	v_lshl_or_b32 v44, v36, 13, v86
	v_mov_b32_e32 v45, 0
	v_lshl_add_u64 v[18:19], s[56:57], 0, v[44:45]
	v_add_co_u32_e32 v34, vcc, 0x1000, v18
	global_load_dwordx4 v[2:5], v44, s[56:57]
	global_load_dwordx4 v[6:9], v44, s[56:57] offset:1024
	global_load_dwordx4 v[10:13], v44, s[56:57] offset:2048
	global_load_dwordx4 v[14:17], v44, s[56:57] offset:3072
	v_addc_co_u32_e32 v35, vcc, 0, v19, vcc
	v_lshlrev_b32_e32 v44, 7, v36
	global_load_dwordx4 v[18:21], v[34:35], off
	global_load_dwordx4 v[22:25], v[34:35], off offset:1024
	global_load_dwordx4 v[26:29], v[34:35], off offset:2048
	global_load_dwordx4 v[30:33], v[34:35], off offset:3072
	v_lshl_add_u64 v[34:35], s[52:53], 0, v[44:45]
	v_lshlrev_b32_e32 v36, 2, v1
	v_mov_b32_e32 v37, v45
	v_lshl_add_u64 v[46:47], v[34:35], 0, v[36:37]
	global_load_dwordx4 v[34:37], v[46:47], off offset:16
	global_load_dwordx4 v[38:41], v[46:47], off
	v_add3_u32 v46, s66, v50, v79
	v_ashrrev_i32_e32 v47, 31, v46
	v_and_b32_e32 v0, 48, v0
	v_lshlrev_b64 v[46:47], 9, v[46:47]
	v_lshlrev_b32_e32 v0, 1, v0
	v_or3_b32 v46, v46, v44, v0
	v_mul_u32_u24_e32 v43, 0x110, v79
	s_movk_i32 s0, 0x1100
	v_lshl_add_u64 v[0:1], s[54:55], 0, v[46:47]
	v_mad_u32_u24 v42, v42, s0, v43
	s_mov_b32 s0, 0x10000
	v_lshl_add_u64 v[0:1], v[0:1], 0, 16
	v_add3_u32 v51, v42, v70, s0
	s_lshr_b32 s74, s74, 6
	s_and_b32 s74, s74, 3
	s_lshl_b32 s75, s74, 2
	s_add_i32 s75, s75, 0x26d50
	s_add_i32 s76, s33, 15
	s_lshr_b32 s76, s76, 4
	v_mov_b64_e32 v[60:61], v[0:1]
	v_mov_b32_e32 v62, v51
	s_mov_b32 s96, 1

.Lep_go:
	s_cmp_eq_u32 s96, 0
	s_cbranch_scc1 .Lep_go2
	s_waitcnt vmcnt(0)
	s_mov_b32 s96, 0
